# speedup vs baseline: 1.0157x; 1.0157x over previous
.Lattn_first_tile:
	v_mov_b32_e32 v71, v69
	s_nop 1
	v_permlane16_swap_b32_e32 v69, v71
	v_max_f32_e32 v69, v69, v71
	v_mov_b32_e32 v71, v69
	s_nop 1
	v_permlane32_swap_b32_e32 v69, v71
	v_max_f32_e32 v69, v69, v71
	v_mov_b32_e32 v80, v69
	v_add_f32_e32 v67, v67, v80
	v_xor_b32_e32 v30, 0x80000000, v67
	v_pk_add_f32 v[46:47], v[46:47], v[80:81] op_sel_hi:[1,0] neg_lo:[0,1] neg_hi:[0,1]
	v_pk_add_f32 v[48:49], v[48:49], v[80:81] op_sel_hi:[1,0] neg_lo:[0,1] neg_hi:[0,1]
	v_pk_add_f32 v[42:43], v[42:43], v[80:81] op_sel_hi:[1,0] neg_lo:[0,1] neg_hi:[0,1]
	v_pk_add_f32 v[44:45], v[44:45], v[80:81] op_sel_hi:[1,0] neg_lo:[0,1] neg_hi:[0,1]
	v_pk_add_f32 v[38:39], v[38:39], v[80:81] op_sel_hi:[1,0] neg_lo:[0,1] neg_hi:[0,1]
	v_pk_add_f32 v[40:41], v[40:41], v[80:81] op_sel_hi:[1,0] neg_lo:[0,1] neg_hi:[0,1]
	v_pk_add_f32 v[34:35], v[34:35], v[80:81] op_sel_hi:[1,0] neg_lo:[0,1] neg_hi:[0,1]
	v_pk_add_f32 v[36:37], v[36:37], v[80:81] op_sel_hi:[1,0] neg_lo:[0,1] neg_hi:[0,1]
	v_mov_b32_e32 v31, v30
	v_mov_b32_e32 v32, v30
	v_mov_b32_e32 v33, v30
	s_branch .Lattn_A_done
